# v100 + k11 combine: the destination-slot / weight loads of all four tokens of a trip issued up front (they gated each token's 12 row loads behind the previous token's rows), counted vmcnt re-derived
# speedup vs baseline: 1.0062x; 1.0062x over previous
.LBB0_1673:
	s_ashr_i32 s51, s50, 31
	s_lshl_b64 s[6:7], s[50:51], 2
	s_add_u32 s8, s2, s6
	s_addc_u32 s9, s3, s7
	global_load_dwordx2 v[136:137], v67, s[8:9]
	s_add_i32 s8, s50, 1
	s_ashr_i32 s9, s8, 31
	s_add_u32 s6, s4, s6
	s_addc_u32 s7, s5, s7
	global_load_dword v36, v67, s[6:7]
	s_lshl_b64 s[6:7], s[8:9], 2
	s_add_u32 s6, s4, s6
	s_addc_u32 s7, s5, s7
	global_load_dword v34, v67, s[6:7]
	s_add_i32 s6, s75, s50
	s_ashr_i32 s7, s6, 31
	s_lshl_b64 s[8:9], s[6:7], 2
	s_add_u32 s10, s2, s8
	s_addc_u32 s11, s3, s9
	global_load_dwordx2 v[68:69], v67, s[10:11]
	s_add_i32 s6, s6, 1
	s_ashr_i32 s7, s6, 31
	s_add_u32 s8, s4, s8
	s_addc_u32 s9, s5, s9
	global_load_dword v52, v67, s[8:9]
	s_lshl_b64 s[6:7], s[6:7], 2
	s_add_u32 s6, s4, s6
	s_addc_u32 s7, s5, s7
	global_load_dword v58, v67, s[6:7]
	v_readlane_b32 s6, v254, 54
	v_readlane_b32 s7, v254, 55
	s_add_i32 s6, s6, s50
	s_ashr_i32 s7, s6, 31
	s_lshl_b64 s[8:9], s[6:7], 2
	s_add_u32 s10, s2, s8
	s_addc_u32 s11, s3, s9
	global_load_dwordx2 v[64:65], v67, s[10:11]
	s_add_i32 s6, s6, 1
	s_ashr_i32 s7, s6, 31
	s_add_u32 s8, s4, s8
	s_addc_u32 s9, s5, s9
	global_load_dword v54, v67, s[8:9]
	s_lshl_b64 s[6:7], s[6:7], 2
	s_add_u32 s6, s4, s6
	s_addc_u32 s7, s5, s7
	global_load_dword v60, v67, s[6:7]
	s_mul_i32 s6, s74, 48
	s_add_i32 s6, s6, s50
	s_ashr_i32 s7, s6, 31
	s_lshl_b64 s[8:9], s[6:7], 2
	s_add_u32 s10, s2, s8
	s_addc_u32 s11, s3, s9
	global_load_dwordx2 v[62:63], v67, s[10:11]
	s_add_i32 s6, s6, 1
	s_ashr_i32 s7, s6, 31
	s_add_u32 s8, s4, s8
	s_addc_u32 s9, s5, s9
	global_load_dword v50, v67, s[8:9]
	s_lshl_b64 s[6:7], s[6:7], 2
	s_add_u32 s6, s4, s6
	s_addc_u32 s7, s5, s7
	global_load_dword v56, v67, s[6:7]
	v_readlane_b32 s6, v253, 4
	s_add_i32 s52, s6, s48
	s_cmpk_lt_i32 s52, 0x4000
	s_cselect_b64 s[40:41], -1, 0
	s_cmpk_gt_i32 s52, 0x3fff
	s_waitcnt vmcnt(11)
	v_ashrrev_i32_e32 v139, 31, v136
	v_mov_b32_e32 v138, v136
	v_lshlrev_b64 v[138:139], 11, v[138:139]
	v_lshl_add_u64 v[156:157], v[40:41], 0, v[138:139]
	v_ashrrev_i32_e32 v139, 31, v137
	v_mov_b32_e32 v138, v137
	v_lshlrev_b64 v[136:137], 11, v[138:139]
	v_lshl_add_u64 v[158:159], v[40:41], 0, v[136:137]
	global_load_dwordx2 v[154:155], v[48:49], off offset:-1536 nt
	global_load_dwordx2 v[152:153], v[156:157], off nt
	global_load_dwordx2 v[150:151], v[158:159], off nt
	global_load_dwordx2 v[148:149], v[48:49], off offset:-1024 nt
	global_load_dwordx2 v[146:147], v[156:157], off offset:512 nt
	global_load_dwordx2 v[144:145], v[158:159], off offset:512 nt
	global_load_dwordx2 v[142:143], v[48:49], off offset:-512 nt
	global_load_dwordx2 v[140:141], v[156:157], off offset:1024 nt
	global_load_dwordx2 v[138:139], v[158:159], off offset:1024 nt
	global_load_dwordx2 v[136:137], v[48:49], off nt
	s_nop 0
	global_load_dwordx2 v[156:157], v[156:157], off offset:1536 nt
	s_nop 0
	global_load_dwordx2 v[158:159], v[158:159], off offset:1536 nt
	s_cbranch_scc1 .LBB0_1675
	s_ashr_i32 s53, s52, 31
	s_lshl_b64 s[6:7], s[52:53], 11
	v_lshl_add_u64 v[110:111], v[38:39], 0, s[6:7]
	s_waitcnt vmcnt(20)
	v_ashrrev_i32_e32 v75, 31, v68
	v_mov_b32_e32 v74, v68
	v_lshlrev_b64 v[74:75], 11, v[74:75]
	v_lshl_add_u64 v[128:129], v[40:41], 0, v[74:75]
	v_ashrrev_i32_e32 v75, 31, v69
	v_mov_b32_e32 v74, v69
	v_lshlrev_b64 v[68:69], 11, v[74:75]
	v_lshl_add_u64 v[134:135], v[40:41], 0, v[68:69]
	global_load_dwordx2 v[68:69], v[110:111], off nt
	global_load_dwordx2 v[74:75], v[128:129], off nt
	global_load_dwordx2 v[80:81], v[134:135], off nt
	global_load_dwordx2 v[86:87], v[110:111], off offset:512 nt
	global_load_dwordx2 v[98:99], v[128:129], off offset:512 nt
	global_load_dwordx2 v[116:117], v[134:135], off offset:512 nt
	global_load_dwordx2 v[94:95], v[110:111], off offset:1024 nt
	global_load_dwordx2 v[112:113], v[128:129], off offset:1024 nt
	global_load_dwordx2 v[122:123], v[134:135], off offset:1024 nt
	s_nop 0
	global_load_dwordx2 v[110:111], v[110:111], off offset:1536 nt
	s_nop 0
	global_load_dwordx2 v[128:129], v[128:129], off offset:1536 nt
	s_nop 0
	global_load_dwordx2 v[134:135], v[134:135], off offset:1536 nt
.LBB0_1675:
	s_add_i32 s44, s75, s48
	s_cmpk_lt_i32 s44, 0x4000
	s_cselect_b64 s[54:55], -1, 0
	s_cmpk_gt_i32 s44, 0x3fff
	s_cbranch_scc1 .LBB0_1677
	s_ashr_i32 s45, s44, 31
	s_lshl_b64 s[6:7], s[44:45], 11
	v_lshl_add_u64 v[106:107], v[38:39], 0, s[6:7]
	s_waitcnt vmcnt(29)
	v_ashrrev_i32_e32 v73, 31, v64
	v_mov_b32_e32 v72, v64
	v_lshlrev_b64 v[72:73], 11, v[72:73]
	v_lshl_add_u64 v[126:127], v[40:41], 0, v[72:73]
	v_ashrrev_i32_e32 v73, 31, v65
	v_mov_b32_e32 v72, v65
	v_lshlrev_b64 v[64:65], 11, v[72:73]
	v_lshl_add_u64 v[132:133], v[40:41], 0, v[64:65]
	global_load_dwordx2 v[64:65], v[106:107], off nt
	global_load_dwordx2 v[72:73], v[126:127], off nt
	global_load_dwordx2 v[78:79], v[132:133], off nt
	global_load_dwordx2 v[84:85], v[106:107], off offset:512 nt
	global_load_dwordx2 v[96:97], v[126:127], off offset:512 nt
	global_load_dwordx2 v[114:115], v[132:133], off offset:512 nt
	global_load_dwordx2 v[92:93], v[106:107], off offset:1024 nt
	global_load_dwordx2 v[108:109], v[126:127], off offset:1024 nt
	global_load_dwordx2 v[120:121], v[132:133], off offset:1024 nt
	s_nop 0
	global_load_dwordx2 v[106:107], v[106:107], off offset:1536 nt
	s_nop 0
	global_load_dwordx2 v[126:127], v[126:127], off offset:1536 nt
	s_nop 0
	global_load_dwordx2 v[132:133], v[132:133], off offset:1536 nt
.LBB0_1677:
	s_mul_i32 s6, s74, 24
	s_add_i32 s34, s6, s48
	s_cmpk_lt_i32 s34, 0x4000
	s_cselect_b64 s[46:47], -1, 0
	s_cmpk_gt_i32 s34, 0x3fff
	s_cbranch_scc1 .LBB0_1679
	s_ashr_i32 s35, s34, 31
	s_lshl_b64 s[6:7], s[34:35], 11
	v_lshl_add_u64 v[100:101], v[38:39], 0, s[6:7]
	s_waitcnt vmcnt(38)
	v_ashrrev_i32_e32 v71, 31, v62
	v_mov_b32_e32 v70, v62
	v_lshlrev_b64 v[70:71], 11, v[70:71]
	v_lshl_add_u64 v[124:125], v[40:41], 0, v[70:71]
	v_ashrrev_i32_e32 v71, 31, v63
	v_mov_b32_e32 v70, v63
	v_lshlrev_b64 v[62:63], 11, v[70:71]
	v_lshl_add_u64 v[130:131], v[40:41], 0, v[62:63]
	global_load_dwordx2 v[62:63], v[100:101], off nt
	global_load_dwordx2 v[70:71], v[124:125], off nt
	global_load_dwordx2 v[76:77], v[130:131], off nt
	global_load_dwordx2 v[82:83], v[100:101], off offset:512 nt
	global_load_dwordx2 v[90:91], v[124:125], off offset:512 nt
	global_load_dwordx2 v[104:105], v[130:131], off offset:512 nt
	global_load_dwordx2 v[88:89], v[100:101], off offset:1024 nt
	global_load_dwordx2 v[102:103], v[124:125], off offset:1024 nt
	global_load_dwordx2 v[118:119], v[130:131], off offset:1024 nt
	s_nop 0
	global_load_dwordx2 v[100:101], v[100:101], off offset:1536 nt
	s_nop 0
	global_load_dwordx2 v[124:125], v[124:125], off offset:1536 nt
	s_nop 0
	global_load_dwordx2 v[130:131], v[130:131], off offset:1536 nt
